# phase-8 tail-fill conversion removed (its tiles go to the attention queue), phase-9 tail-fill kept
# speedup vs baseline: 1.0025x; 1.0025x over previous
.LBB0_789:
	s_or_b64 exec, exec, s[2:3]
	v_readlane_b32 s2, v253, 55
	s_waitcnt lgkmcnt(0)
	s_barrier
	v_mov_b32_e32 v0, s2
	v_readlane_b32 s2, v253, 54
	ds_read_b32 v0, v0
	s_nop 0
	v_mov_b32_e32 v1, s2
	ds_read_b32 v1, v1
	s_waitcnt lgkmcnt(0)
	s_barrier
	v_add_u32_e32 v201, 0x580, v0
	s_nop 0
	v_readfirstlane_b32 s100, v201
	v_readlane_b32 s101, v254, 38
	s_nop 3
	s_movk_i32 vcc_lo, 0x540
	s_movk_i32 vcc_hi, 0xd20
	s_cmp_eq_u32 s101, 0
	s_cselect_b32 vcc_lo, 0x600, vcc_lo
	s_cselect_b32 vcc_hi, 0xf00, vcc_hi
	s_add_i32 vcc_lo, s100, vcc_lo
	s_max_u32 vcc_lo, vcc_lo, vcc_hi
	v_mov_b32_e32 v201, vcc_lo
	v_readfirstlane_b32 s30, v0
	v_cmp_ge_i32_e32 vcc, v1, v201
	v_readfirstlane_b32 s24, v1
	s_cbranch_vccnz .LBB0_931
	s_add_u32 s31, s4, 0x37b00000
	s_addc_u32 s34, s5, 0
	s_add_i32 s35, s30, 0x480
	s_add_u32 s44, s4, 0x61800000
	s_addc_u32 s45, s5, 0
	s_add_u32 s46, s4, 0x42c00000
	s_addc_u32 s47, s5, 0
	s_add_u32 s10, s4, 0x66d00000
	s_addc_u32 s11, s5, 0
	s_add_u32 s48, s4, 0x61640000
	s_movk_i32 s2, 0x100
	s_addc_u32 s49, s5, 0
	v_cmp_gt_i32_e64 s[38:39], s2, v199
	s_add_i32 s2, 0, 0x14800
	v_add_u32_e32 v214, s2, v200
	s_add_i32 s2, 0, 0x16800
	s_cmp_lg_u32 0, -1
	v_lshlrev_b32_e32 v3, 1, v199
	v_lshlrev_b32_e32 v211, 4, v199
	s_cselect_b32 s3, 0, 0
	v_lshlrev_b32_e32 v0, 3, v199
	v_lshlrev_b32_e32 v1, 10, v101
	v_lshlrev_b32_e32 v2, 4, v198
	v_and_b32_e32 v3, 32, v3
	v_and_b32_e32 v5, 0xc0, v211
	s_addk_i32 s3, 0x6000
	v_and_b32_e32 v210, 24, v0
	v_lshl_or_b32 v5, v101, 8, v5
	v_add3_u32 v213, 0, v1, v2
	v_add_u32_e32 v1, s3, v3
	v_add3_u32 v217, v1, v210, v5
	v_lshrrev_b32_e32 v1, 3, v100
	v_lshl_add_u32 v215, v198, 2, s2
	v_and_b32_e32 v218, 56, v0
	v_lshl_add_u32 v220, v1, 2, s2
	s_add_i32 s2, 0, 0x14a00
	v_add_u32_e32 v4, 0, v3
	v_lshlrev_b32_e32 v96, 1, v218
	v_add_u32_e32 v221, s2, v200
	s_add_i32 s2, 0, 0x14900
	v_ashrrev_i32_e32 v203, 31, v202
	v_lshlrev_b32_e32 v208, 9, v100
	v_lshrrev_b32_e32 v209, 2, v100
	v_add3_u32 v212, v4, v210, v5
	v_cmp_gt_u32_e64 s[40:41], 32, v100
	v_cmp_lt_u32_e64 s[42:43], 31, v100
	v_or_b32_e32 v216, 0xc0, v206
	v_lshl_add_u64 v[204:205], s[4:5], 0, v[96:97]
	v_lshlrev_b32_e32 v219, 7, v1
	v_add_u32_e32 v222, s2, v200
	v_lshlrev_b32_e32 v96, 1, v98
	s_branch .LBB0_792

.LBB0_796:
	s_or_b64 exec, exec, s[2:3]
	v_readlane_b32 s101, v254, 38
	s_nop 3
	s_cmp_eq_u32 s101, 0
	s_cbranch_scc1 .Lc3_l0
	s_cmpk_lt_u32 s24, 0xd20
	s_cbranch_scc0 .Lc3_late

.Lc3_late:
	s_sub_i32 s24, s24, 0x540
	s_branch .Lc3_chk

.Lc3_nextl:
	s_lshl_b32 s19, s101, 3
	s_add_i32 s19, s19, s2
	s_cmpk_lt_u32 s101, 0x80
	s_cbranch_scc1 .Lc3_have
	s_addk_i32 s19, 0x600
